# Q-projection GEMM rotary epilogue: the cos/sin rows of all 8 row groups of a tile touched up front so the per-unit load-wait-store ladder hits cache
# speedup vs baseline: 1.0036x; 1.0016x over previous
.LBB0_231:
	s_add_u32 s50, vcc_lo, 0xfff80080
	s_addc_u32 s51, vcc_hi, -1
	s_add_i32 s64, 0, 0x10000
	v_add_u32_e32 v96, s64, v141
	ds_read_b128 v[150:153], v96
	ds_read_b128 v[154:157], v96 offset:1024
	ds_read_b128 v[158:161], v96 offset:2048
	ds_read_b128 v[174:177], v96 offset:3072
	s_cmp_eq_u32 s96, 28
	s_cselect_b32 s93, s37, s51
	s_cselect_b32 s92, s49, s50
	s_cselect_b32 s51, s45, s24
	s_cselect_b32 s50, s14, s10
	v_lshl_add_u64 v[212:213], vcc, 0, v[146:147]
	s_add_i32 m0, s21, 0xc000
	ds_read_b128 v[180:183], v178
	ds_read_b128 v[184:187], v178 offset:1024
	ds_read_b128 v[188:191], v178 offset:2048
	ds_read_b128 v[192:195], v178 offset:3072
	ds_read_b128 v[196:199], v178 offset:4096
	ds_read_b128 v[200:203], v178 offset:5120
	ds_read_b128 v[206:209], v178 offset:6144
	ds_read_b128 v[228:231], v178 offset:7168
	global_load_lds_dwordx4 v[212:213], off
	v_lshl_add_u64 v[212:213], vcc, 0, v[148:149]
	s_add_i32 m0, s21, 0xe000
	s_nop 0
	global_load_lds_dwordx4 v[212:213], off
	s_waitcnt lgkmcnt(8)
	s_barrier
	s_waitcnt lgkmcnt(0)
	s_setprio 1
	s_waitcnt lgkmcnt(0)
	v_mfma_f32_16x16x32_bf16 v[126:129], v[150:153], v[180:183], v[126:129]
	v_mfma_f32_16x16x32_bf16 v[122:125], v[158:161], v[180:183], v[122:125]
	v_mfma_f32_16x16x32_bf16 v[118:121], v[150:153], v[188:191], v[118:121]
	v_mfma_f32_16x16x32_bf16 v[114:117], v[158:161], v[188:191], v[114:117]
	v_mfma_f32_16x16x32_bf16 v[102:105], v[150:153], v[196:199], v[102:105]
	v_mfma_f32_16x16x32_bf16 v[98:101], v[158:161], v[196:199], v[98:101]
	v_mfma_f32_16x16x32_bf16 v[84:87], v[150:153], v[206:209], v[84:87]
	v_mfma_f32_16x16x32_bf16 v[80:83], v[158:161], v[206:209], v[80:83]
	v_mfma_f32_16x16x32_bf16 v[126:129], v[154:157], v[184:187], v[126:129]
	v_mfma_f32_16x16x32_bf16 v[122:125], v[174:177], v[184:187], v[122:125]
	v_mfma_f32_16x16x32_bf16 v[118:121], v[154:157], v[192:195], v[118:121]
	v_mfma_f32_16x16x32_bf16 v[114:117], v[174:177], v[192:195], v[114:117]
	v_mfma_f32_16x16x32_bf16 v[102:105], v[154:157], v[200:203], v[102:105]
	v_mfma_f32_16x16x32_bf16 v[98:101], v[174:177], v[200:203], v[98:101]
	v_mfma_f32_16x16x32_bf16 v[84:87], v[154:157], v[228:231], v[84:87]
	v_mfma_f32_16x16x32_bf16 v[80:83], v[174:177], v[228:231], v[80:83]
	s_setprio 0
	s_barrier
	s_add_i32 s66, 0, 0x14000
	s_add_i32 s64, s64, s9
	v_add_u32_e32 v96, s66, v141
	v_lshl_add_u64 v[212:213], s[50:51], 0, v[132:133]
	s_mov_b32 m0, s64
	ds_read_b128 v[232:235], v96
	ds_read_b128 v[236:239], v96 offset:1024
	ds_read_b128 v[240:243], v96 offset:2048
	ds_read_b128 v[244:247], v96 offset:3072
	global_load_lds_dwordx4 v[212:213], off
	v_lshl_add_u64 v[248:249], s[50:51], 0, v[136:137]
	s_add_i32 m0, s64, 0x2000
	s_nop 0
	global_load_lds_dwordx4 v[248:249], off
	s_barrier
	s_waitcnt lgkmcnt(0)
	s_setprio 1
	s_waitcnt lgkmcnt(0)
	v_mfma_f32_16x16x32_bf16 v[110:113], v[232:235], v[180:183], v[110:113]
	v_mfma_f32_16x16x32_bf16 v[106:109], v[240:243], v[180:183], v[106:109]
	v_mfma_f32_16x16x32_bf16 v[92:95], v[232:235], v[188:191], v[92:95]
	v_mfma_f32_16x16x32_bf16 v[88:91], v[240:243], v[188:191], v[88:91]
	v_mfma_f32_16x16x32_bf16 v[76:79], v[232:235], v[196:199], v[76:79]
	v_mfma_f32_16x16x32_bf16 v[72:75], v[240:243], v[196:199], v[72:75]
	v_mfma_f32_16x16x32_bf16 v[68:71], v[232:235], v[206:209], v[68:71]
	v_mfma_f32_16x16x32_bf16 v[64:67], v[240:243], v[206:209], v[64:67]
	v_mfma_f32_16x16x32_bf16 v[110:113], v[236:239], v[184:187], v[110:113]
	v_mfma_f32_16x16x32_bf16 v[106:109], v[244:247], v[184:187], v[106:109]
	v_mfma_f32_16x16x32_bf16 v[92:95], v[236:239], v[192:195], v[92:95]
	v_mfma_f32_16x16x32_bf16 v[88:91], v[244:247], v[192:195], v[88:91]
	v_mfma_f32_16x16x32_bf16 v[76:79], v[236:239], v[200:203], v[76:79]
	v_mfma_f32_16x16x32_bf16 v[72:75], v[244:247], v[200:203], v[72:75]
	v_mfma_f32_16x16x32_bf16 v[68:71], v[236:239], v[228:231], v[68:71]
	v_mfma_f32_16x16x32_bf16 v[64:67], v[244:247], v[228:231], v[64:67]
	s_setprio 0
	s_mov_b32 m0, s21
	v_lshl_add_u64 v[250:251], s[92:93], 0, v[130:131]
	s_barrier
	ds_read_b128 v[180:183], v178 offset:16384
	ds_read_b128 v[184:187], v178 offset:17408
	ds_read_b128 v[188:191], v178 offset:18432
	ds_read_b128 v[192:195], v178 offset:19456
	ds_read_b128 v[196:199], v178 offset:20480
	ds_read_b128 v[200:203], v178 offset:21504
	ds_read_b128 v[206:209], v178 offset:22528
	ds_read_b128 v[228:231], v178 offset:23552
	global_load_lds_dwordx4 v[250:251], off
	v_lshl_add_u64 v[252:253], s[92:93], 0, v[134:135]
	s_mov_b32 m0, s38
	s_nop 0
	global_load_lds_dwordx4 v[252:253], off
	s_barrier
	s_waitcnt lgkmcnt(0)
	s_setprio 1
	s_waitcnt lgkmcnt(0)
	v_mfma_f32_16x16x32_bf16 v[60:63], v[150:153], v[180:183], v[60:63]
	v_mfma_f32_16x16x32_bf16 v[56:59], v[158:161], v[180:183], v[56:59]
	v_mfma_f32_16x16x32_bf16 v[52:55], v[150:153], v[188:191], v[52:55]
	v_mfma_f32_16x16x32_bf16 v[48:51], v[158:161], v[188:191], v[48:51]
	v_mfma_f32_16x16x32_bf16 v[36:39], v[150:153], v[196:199], v[36:39]
	v_mfma_f32_16x16x32_bf16 v[32:35], v[158:161], v[196:199], v[32:35]
	v_mfma_f32_16x16x32_bf16 v[20:23], v[150:153], v[206:209], v[20:23]
	v_mfma_f32_16x16x32_bf16 v[16:19], v[158:161], v[206:209], v[16:19]
	v_mfma_f32_16x16x32_bf16 v[60:63], v[154:157], v[184:187], v[60:63]
	v_mfma_f32_16x16x32_bf16 v[56:59], v[174:177], v[184:187], v[56:59]
	v_mfma_f32_16x16x32_bf16 v[52:55], v[154:157], v[192:195], v[52:55]
	v_mfma_f32_16x16x32_bf16 v[48:51], v[174:177], v[192:195], v[48:51]
	v_mfma_f32_16x16x32_bf16 v[36:39], v[154:157], v[200:203], v[36:39]
	v_mfma_f32_16x16x32_bf16 v[32:35], v[174:177], v[200:203], v[32:35]
	v_mfma_f32_16x16x32_bf16 v[20:23], v[154:157], v[228:231], v[20:23]
	v_mfma_f32_16x16x32_bf16 v[16:19], v[174:177], v[228:231], v[16:19]
	s_setprio 0
	s_barrier
	s_add_u32 s64, s50, 0x80000
	s_addc_u32 s65, s51, 0
	s_add_i32 s66, s66, s9
	v_lshl_add_u64 v[150:151], s[64:65], 0, v[132:133]
	s_mov_b32 m0, s66
	s_nop 0
	global_load_lds_dwordx4 v[150:151], off
	v_lshl_add_u64 v[150:151], s[64:65], 0, v[136:137]
	s_add_i32 m0, s66, 0x2000
	s_nop 0
	global_load_lds_dwordx4 v[150:151], off
	s_waitcnt vmcnt(6)
	s_barrier
	s_setprio 1
	v_mfma_f32_16x16x32_bf16 v[44:47], v[232:235], v[180:183], v[44:47]
	v_mfma_f32_16x16x32_bf16 v[40:43], v[240:243], v[180:183], v[40:43]
	v_mfma_f32_16x16x32_bf16 v[28:31], v[232:235], v[188:191], v[28:31]
	v_mfma_f32_16x16x32_bf16 v[24:27], v[240:243], v[188:191], v[24:27]
	v_mfma_f32_16x16x32_bf16 v[12:15], v[232:235], v[196:199], v[12:15]
	v_mfma_f32_16x16x32_bf16 v[8:11], v[240:243], v[196:199], v[8:11]
	v_mfma_f32_16x16x32_bf16 v[4:7], v[232:235], v[206:209], v[4:7]
	v_mfma_f32_16x16x32_bf16 v[0:3], v[240:243], v[206:209], v[0:3]
	v_mfma_f32_16x16x32_bf16 v[44:47], v[236:239], v[184:187], v[44:47]
	v_mfma_f32_16x16x32_bf16 v[40:43], v[244:247], v[184:187], v[40:43]
	v_mfma_f32_16x16x32_bf16 v[28:31], v[236:239], v[192:195], v[28:31]
	v_mfma_f32_16x16x32_bf16 v[24:27], v[244:247], v[192:195], v[24:27]
	v_mfma_f32_16x16x32_bf16 v[12:15], v[236:239], v[200:203], v[12:15]
	v_mfma_f32_16x16x32_bf16 v[8:11], v[244:247], v[200:203], v[8:11]
	v_mfma_f32_16x16x32_bf16 v[4:7], v[236:239], v[228:231], v[4:7]
	v_mfma_f32_16x16x32_bf16 v[0:3], v[244:247], v[228:231], v[0:3]
	s_setprio 0
	s_add_i32 s66, 0, 0x18000
	v_add_u32_e32 v96, s66, v141
	s_barrier
	ds_read_b128 v[150:153], v96
	ds_read_b128 v[154:157], v96 offset:1024
	ds_read_b128 v[158:161], v96 offset:2048
	ds_read_b128 v[174:177], v96 offset:3072
	s_add_u32 s64, s92, 0x80000
	s_addc_u32 s65, s93, 0
	s_mov_b32 m0, s39
	v_lshl_add_u64 v[232:233], s[64:65], 0, v[130:131]
	ds_read_b128 v[180:183], v178 offset:32768
	ds_read_b128 v[184:187], v178 offset:33792
	ds_read_b128 v[188:191], v178 offset:34816
	ds_read_b128 v[192:195], v178 offset:35840
	ds_read_b128 v[196:199], v178 offset:36864
	ds_read_b128 v[200:203], v178 offset:37888
	ds_read_b128 v[206:209], v178 offset:38912
	ds_read_b128 v[228:231], v178 offset:39936
	global_load_lds_dwordx4 v[232:233], off
	v_lshl_add_u64 v[232:233], s[64:65], 0, v[134:135]
	s_mov_b32 m0, s82
	s_nop 0
	global_load_lds_dwordx4 v[232:233], off
	s_waitcnt lgkmcnt(8)
	s_barrier
	s_waitcnt lgkmcnt(0)
	s_setprio 1
	s_waitcnt lgkmcnt(0)
	v_mfma_f32_16x16x32_bf16 v[126:129], v[150:153], v[180:183], v[126:129]
	v_mfma_f32_16x16x32_bf16 v[122:125], v[158:161], v[180:183], v[122:125]
	v_mfma_f32_16x16x32_bf16 v[118:121], v[150:153], v[188:191], v[118:121]
	v_mfma_f32_16x16x32_bf16 v[114:117], v[158:161], v[188:191], v[114:117]
	v_mfma_f32_16x16x32_bf16 v[102:105], v[150:153], v[196:199], v[102:105]
	v_mfma_f32_16x16x32_bf16 v[98:101], v[158:161], v[196:199], v[98:101]
	v_mfma_f32_16x16x32_bf16 v[84:87], v[150:153], v[206:209], v[84:87]
	v_mfma_f32_16x16x32_bf16 v[80:83], v[158:161], v[206:209], v[80:83]
	v_mfma_f32_16x16x32_bf16 v[126:129], v[154:157], v[184:187], v[126:129]
	v_mfma_f32_16x16x32_bf16 v[122:125], v[174:177], v[184:187], v[122:125]
	v_mfma_f32_16x16x32_bf16 v[118:121], v[154:157], v[192:195], v[118:121]
	v_mfma_f32_16x16x32_bf16 v[114:117], v[174:177], v[192:195], v[114:117]
	v_mfma_f32_16x16x32_bf16 v[102:105], v[154:157], v[200:203], v[102:105]
	v_mfma_f32_16x16x32_bf16 v[98:101], v[174:177], v[200:203], v[98:101]
	v_mfma_f32_16x16x32_bf16 v[84:87], v[154:157], v[228:231], v[84:87]
	v_mfma_f32_16x16x32_bf16 v[80:83], v[174:177], v[228:231], v[80:83]
	s_setprio 0
	s_barrier
	s_add_i32 s64, 0, 0x1c000
	s_add_i32 s65, s66, s9
	v_add_u32_e32 v96, s64, v141
	v_lshl_add_u64 v[212:213], v[212:213], 0, s[18:19]
	s_mov_b32 m0, s65
	ds_read_b128 v[232:235], v96
	ds_read_b128 v[236:239], v96 offset:1024
	ds_read_b128 v[240:243], v96 offset:2048
	ds_read_b128 v[244:247], v96 offset:3072
	global_load_lds_dwordx4 v[212:213], off
	v_lshl_add_u64 v[212:213], v[248:249], 0, s[18:19]
	s_add_i32 m0, s65, 0x2000
	s_nop 0
	global_load_lds_dwordx4 v[212:213], off
	s_barrier
	s_waitcnt lgkmcnt(0)
	s_setprio 1
	s_waitcnt lgkmcnt(0)
	v_mfma_f32_16x16x32_bf16 v[110:113], v[232:235], v[180:183], v[110:113]
	v_mfma_f32_16x16x32_bf16 v[106:109], v[240:243], v[180:183], v[106:109]
	v_mfma_f32_16x16x32_bf16 v[92:95], v[232:235], v[188:191], v[92:95]
	v_mfma_f32_16x16x32_bf16 v[88:91], v[240:243], v[188:191], v[88:91]
	v_mfma_f32_16x16x32_bf16 v[76:79], v[232:235], v[196:199], v[76:79]
	v_mfma_f32_16x16x32_bf16 v[72:75], v[240:243], v[196:199], v[72:75]
	v_mfma_f32_16x16x32_bf16 v[68:71], v[232:235], v[206:209], v[68:71]
	v_mfma_f32_16x16x32_bf16 v[64:67], v[240:243], v[206:209], v[64:67]
	v_mfma_f32_16x16x32_bf16 v[110:113], v[236:239], v[184:187], v[110:113]
	v_mfma_f32_16x16x32_bf16 v[106:109], v[244:247], v[184:187], v[106:109]
	v_mfma_f32_16x16x32_bf16 v[92:95], v[236:239], v[192:195], v[92:95]
	v_mfma_f32_16x16x32_bf16 v[88:91], v[244:247], v[192:195], v[88:91]
	v_mfma_f32_16x16x32_bf16 v[76:79], v[236:239], v[200:203], v[76:79]
	v_mfma_f32_16x16x32_bf16 v[72:75], v[244:247], v[200:203], v[72:75]
	v_mfma_f32_16x16x32_bf16 v[68:71], v[236:239], v[228:231], v[68:71]
	v_mfma_f32_16x16x32_bf16 v[64:67], v[244:247], v[228:231], v[64:67]
	s_setprio 0
	s_mov_b32 m0, s84
	v_lshl_add_u64 v[212:213], v[250:251], 0, s[18:19]
	s_barrier
	ds_read_b128 v[180:183], v178 offset:49152
	ds_read_b128 v[184:187], v178 offset:50176
	ds_read_b128 v[188:191], v178 offset:51200
	ds_read_b128 v[192:195], v178 offset:52224
	ds_read_b128 v[196:199], v178 offset:53248
	ds_read_b128 v[200:203], v178 offset:54272
	ds_read_b128 v[206:209], v178 offset:55296
	ds_read_b128 v[228:231], v178 offset:56320
	global_load_lds_dwordx4 v[212:213], off
	v_lshl_add_u64 v[212:213], v[252:253], 0, s[18:19]
	s_mov_b32 m0, s89
	s_nop 0
	global_load_lds_dwordx4 v[212:213], off
	s_barrier
	s_waitcnt lgkmcnt(0)
	s_setprio 1
	s_waitcnt lgkmcnt(0)
	v_mfma_f32_16x16x32_bf16 v[60:63], v[150:153], v[180:183], v[60:63]
	v_mfma_f32_16x16x32_bf16 v[56:59], v[158:161], v[180:183], v[56:59]
	v_mfma_f32_16x16x32_bf16 v[52:55], v[150:153], v[188:191], v[52:55]
	v_mfma_f32_16x16x32_bf16 v[48:51], v[158:161], v[188:191], v[48:51]
	v_mfma_f32_16x16x32_bf16 v[36:39], v[150:153], v[196:199], v[36:39]
	v_mfma_f32_16x16x32_bf16 v[32:35], v[158:161], v[196:199], v[32:35]
	v_mfma_f32_16x16x32_bf16 v[20:23], v[150:153], v[206:209], v[20:23]
	v_mfma_f32_16x16x32_bf16 v[16:19], v[158:161], v[206:209], v[16:19]
	v_mfma_f32_16x16x32_bf16 v[60:63], v[154:157], v[184:187], v[60:63]
	v_mfma_f32_16x16x32_bf16 v[56:59], v[174:177], v[184:187], v[56:59]
	v_mfma_f32_16x16x32_bf16 v[52:55], v[154:157], v[192:195], v[52:55]
	v_mfma_f32_16x16x32_bf16 v[48:51], v[174:177], v[192:195], v[48:51]
	v_mfma_f32_16x16x32_bf16 v[36:39], v[154:157], v[200:203], v[36:39]
	v_mfma_f32_16x16x32_bf16 v[32:35], v[174:177], v[200:203], v[32:35]
	v_mfma_f32_16x16x32_bf16 v[20:23], v[154:157], v[228:231], v[20:23]
	v_mfma_f32_16x16x32_bf16 v[16:19], v[174:177], v[228:231], v[16:19]
	s_setprio 0
	s_barrier
	s_add_u32 s50, s50, 0x80080
	s_addc_u32 s51, s51, 0
	s_add_i32 s64, s64, s9
	v_lshl_add_u64 v[150:151], s[50:51], 0, v[132:133]
	s_mov_b32 m0, s64
	s_nop 0
	global_load_lds_dwordx4 v[150:151], off
	v_lshl_add_u64 v[150:151], s[50:51], 0, v[136:137]
	s_add_i32 m0, s64, 0x2000
	s_nop 0
	global_load_lds_dwordx4 v[150:151], off
	s_waitcnt vmcnt(6)
	s_barrier
	s_setprio 1
	v_mfma_f32_16x16x32_bf16 v[44:47], v[232:235], v[180:183], v[44:47]
	v_mfma_f32_16x16x32_bf16 v[40:43], v[240:243], v[180:183], v[40:43]
	v_mfma_f32_16x16x32_bf16 v[28:31], v[232:235], v[188:191], v[28:31]
	v_mfma_f32_16x16x32_bf16 v[24:27], v[240:243], v[188:191], v[24:27]
	v_mfma_f32_16x16x32_bf16 v[12:15], v[232:235], v[196:199], v[12:15]
	v_mfma_f32_16x16x32_bf16 v[8:11], v[240:243], v[196:199], v[8:11]
	v_mfma_f32_16x16x32_bf16 v[4:7], v[232:235], v[206:209], v[4:7]
	v_mfma_f32_16x16x32_bf16 v[0:3], v[240:243], v[206:209], v[0:3]
	v_mfma_f32_16x16x32_bf16 v[44:47], v[236:239], v[184:187], v[44:47]
	v_mfma_f32_16x16x32_bf16 v[40:43], v[244:247], v[184:187], v[40:43]
	v_mfma_f32_16x16x32_bf16 v[28:31], v[236:239], v[192:195], v[28:31]
	v_mfma_f32_16x16x32_bf16 v[24:27], v[244:247], v[192:195], v[24:27]
	v_mfma_f32_16x16x32_bf16 v[12:15], v[236:239], v[200:203], v[12:15]
	v_mfma_f32_16x16x32_bf16 v[8:11], v[244:247], v[200:203], v[8:11]
	v_mfma_f32_16x16x32_bf16 v[4:7], v[236:239], v[228:231], v[4:7]
	v_mfma_f32_16x16x32_bf16 v[0:3], v[244:247], v[228:231], v[0:3]
	s_setprio 0
	s_add_i32 s96, s96, 2
	s_add_u32 vcc_lo, vcc_lo, 0x100
	s_addc_u32 vcc_hi, vcc_hi, 0
	s_add_u32 s10, s10, 0x100
	s_addc_u32 s24, s24, 0
	s_cmp_gt_u32 s96, 29
	s_barrier
	s_cbranch_scc0 .LBB0_231
	s_lshl_b32 s10, s36, 8
	s_add_i32 s10, s10, s83
	s_lshl_b32 s45, s88, 8
	v_or_b32_e32 v150, s10, v139
	v_or_b32_e32 v152, s45, v138
	s_andn2_b64 vcc, exec, s[34:35]
	s_mov_b64 s[36:37], -1
	s_cbranch_vccnz .LBB0_284
	v_lshlrev_b32_e32 v228, 8, v150
	v_mov_b32_e32 v229, 0
	v_mov_b32_e32 v231, 0
	v_lshl_add_u64 v[232:233], v[142:143], 0, v[228:229]
	global_load_dword v236, v[232:233], off
	v_lshl_add_u64 v[234:235], v[144:145], 0, v[228:229]
	global_load_dword v236, v[234:235], off
	v_add_u32_e32 v230, 0x1000, v228
	v_lshl_add_u64 v[232:233], v[142:143], 0, v[230:231]
	global_load_dword v236, v[232:233], off
	v_lshl_add_u64 v[234:235], v[144:145], 0, v[230:231]
	global_load_dword v236, v[234:235], off
	v_add_u32_e32 v230, 0x2000, v228
	v_lshl_add_u64 v[232:233], v[142:143], 0, v[230:231]
	global_load_dword v236, v[232:233], off
	v_lshl_add_u64 v[234:235], v[144:145], 0, v[230:231]
	global_load_dword v236, v[234:235], off
	v_add_u32_e32 v230, 0x3000, v228
	v_lshl_add_u64 v[232:233], v[142:143], 0, v[230:231]
	global_load_dword v236, v[232:233], off
	v_lshl_add_u64 v[234:235], v[144:145], 0, v[230:231]
	global_load_dword v236, v[234:235], off
	v_add_u32_e32 v230, 0x8000, v228
	v_lshl_add_u64 v[232:233], v[142:143], 0, v[230:231]
	global_load_dword v236, v[232:233], off
	v_lshl_add_u64 v[234:235], v[144:145], 0, v[230:231]
	global_load_dword v236, v[234:235], off
	v_add_u32_e32 v230, 0x9000, v228
	v_lshl_add_u64 v[232:233], v[142:143], 0, v[230:231]
	global_load_dword v236, v[232:233], off
	v_lshl_add_u64 v[234:235], v[144:145], 0, v[230:231]
	global_load_dword v236, v[234:235], off
	v_add_u32_e32 v230, 0xa000, v228
	v_lshl_add_u64 v[232:233], v[142:143], 0, v[230:231]
	global_load_dword v236, v[232:233], off
	v_lshl_add_u64 v[234:235], v[144:145], 0, v[230:231]
	global_load_dword v236, v[234:235], off
	v_add_u32_e32 v230, 0xb000, v228
	v_lshl_add_u64 v[232:233], v[142:143], 0, v[230:231]
	global_load_dword v236, v[232:233], off
	v_lshl_add_u64 v[234:235], v[144:145], 0, v[230:231]
	global_load_dword v236, v[234:235], off
	s_ashr_i32 s10, s10, 9
	v_lshlrev_b32_e32 v96, 7, v150
	s_and_b32 s49, s10, -16
	v_and_b32_e32 v153, 0xfe780, v96
	v_cmp_le_i32_e32 vcc, s2, v152
	v_lshlrev_b32_e32 v154, 1, v138
	s_and_saveexec_b64 s[36:37], vcc
	s_xor_b64 s[36:37], exec, s[36:37]
	s_cbranch_execz .LBB0_235
	s_sub_i32 s10, s45, s2
	s_lshr_b32 s10, s10, 7
	s_add_i32 s50, s49, s10
	s_ashr_i32 s51, s50, 31
	s_lshl_b64 s[50:51], s[50:51], 21
	v_lshl_or_b32 v160, v153, 1, s50
	v_mov_b32_e32 v161, s51
	v_mov_b32_e32 v155, v97
	v_cvt_pk_bf16_f32 v156, v126, v127
	v_cvt_pk_bf16_f32 v157, v128, v129
	v_cvt_pk_bf16_f32 v158, v122, v123
	v_cvt_pk_bf16_f32 v159, v124, v125
	v_lshl_add_u64 v[160:161], v[160:161], 0, v[154:155]
	flat_store_dwordx4 v[160:161], v[156:159]
